# v50 + the 64 serialized LDS read-modify-writes of the gated-sum accumulation (two sites per NSA unit) batched 4-wide and software-pipelined; same arithmetic
# speedup vs baseline: 1.0127x; 1.0049x over previous
.LBB0_1645:
	s_or_b64 exec, exec, s[4:5]
	v_lshlrev_b32_e32 v1, 2, v68
	v_lshl_add_u32 v0, v2, 1, s72
	v_or_b32_e32 v72, s48, v1
	s_waitcnt lgkmcnt(0)
	v_lshl_add_u32 v2, v68, 4, s45
	v_mad_u64_u32 v[72:73], s[4:5], v72, s71, v[0:1]
	v_readlane_b32 s8, v255, 11
	v_readlane_b32 s1, v255, 10
	s_or_b32 s8, s8, s1
	s_movk_i32 s1, 0x88
	v_readlane_b32 s9, v255, 12
	v_readlane_b32 s6, v254, 36
	v_readlane_b32 s3, v255, 9
	v_readlane_b32 s7, v254, 37
	ds_read_b128 v[180:183], v2
	ds_read_b128 v[184:187], v2 offset:32
	ds_read_b128 v[188:191], v2 offset:64
	ds_read_b128 v[192:195], v2 offset:96
	ds_read_u16 v196, v72 offset:0
	ds_read_u16 v197, v72 offset:64
	ds_read_u16 v198, v72 offset:128
	ds_read_u16 v199, v72 offset:192
	ds_read_u16 v200, v72 offset:272
	ds_read_u16 v201, v72 offset:336
	ds_read_u16 v202, v72 offset:400
	ds_read_u16 v203, v72 offset:464
	s_waitcnt lgkmcnt(4)
	v_lshlrev_b32_e32 v196, 16, v196
	v_lshlrev_b32_e32 v197, 16, v197
	v_lshlrev_b32_e32 v198, 16, v198
	v_lshlrev_b32_e32 v199, 16, v199
	v_fmac_f32_e32 v196, v20, v180
	v_fmac_f32_e32 v197, v36, v180
	v_fmac_f32_e32 v198, v52, v180
	v_fmac_f32_e32 v199, v4, v180
	v_bfe_u32 v204, v196, 16, 1
	v_bfe_u32 v205, v197, 16, 1
	v_bfe_u32 v206, v198, 16, 1
	v_bfe_u32 v207, v199, 16, 1
	v_add3_u32 v196, v196, v204, s96
	v_add3_u32 v197, v197, v205, s96
	v_add3_u32 v198, v198, v206, s96
	v_add3_u32 v199, v199, v207, s96
	ds_write_b16_d16_hi v72, v196 offset:0
	ds_write_b16_d16_hi v72, v197 offset:64
	ds_write_b16_d16_hi v72, v198 offset:128
	ds_write_b16_d16_hi v72, v199 offset:192
	ds_read_u16 v196, v72 offset:544
	ds_read_u16 v197, v72 offset:608
	ds_read_u16 v198, v72 offset:672
	ds_read_u16 v199, v72 offset:736
	s_waitcnt lgkmcnt(4)
	v_lshlrev_b32_e32 v200, 16, v200
	v_lshlrev_b32_e32 v201, 16, v201
	v_lshlrev_b32_e32 v202, 16, v202
	v_lshlrev_b32_e32 v203, 16, v203
	v_fmac_f32_e32 v200, v21, v181
	v_fmac_f32_e32 v201, v37, v181
	v_fmac_f32_e32 v202, v53, v181
	v_fmac_f32_e32 v203, v5, v181
	v_bfe_u32 v204, v200, 16, 1
	v_bfe_u32 v205, v201, 16, 1
	v_bfe_u32 v206, v202, 16, 1
	v_bfe_u32 v207, v203, 16, 1
	v_add3_u32 v200, v200, v204, s96
	v_add3_u32 v201, v201, v205, s96
	v_add3_u32 v202, v202, v206, s96
	v_add3_u32 v203, v203, v207, s96
	ds_write_b16_d16_hi v72, v200 offset:272
	ds_write_b16_d16_hi v72, v201 offset:336
	ds_write_b16_d16_hi v72, v202 offset:400
	ds_write_b16_d16_hi v72, v203 offset:464
	ds_read_u16 v200, v72 offset:816
	ds_read_u16 v201, v72 offset:880
	ds_read_u16 v202, v72 offset:944
	ds_read_u16 v203, v72 offset:1008
	s_waitcnt lgkmcnt(4)
	v_lshlrev_b32_e32 v196, 16, v196
	v_lshlrev_b32_e32 v197, 16, v197
	v_lshlrev_b32_e32 v198, 16, v198
	v_lshlrev_b32_e32 v199, 16, v199
	v_fmac_f32_e32 v196, v22, v182
	v_fmac_f32_e32 v197, v38, v182
	v_fmac_f32_e32 v198, v54, v182
	v_fmac_f32_e32 v199, v6, v182
	v_bfe_u32 v204, v196, 16, 1
	v_bfe_u32 v205, v197, 16, 1
	v_bfe_u32 v206, v198, 16, 1
	v_bfe_u32 v207, v199, 16, 1
	v_add3_u32 v196, v196, v204, s96
	v_add3_u32 v197, v197, v205, s96
	v_add3_u32 v198, v198, v206, s96
	v_add3_u32 v199, v199, v207, s96
	ds_write_b16_d16_hi v72, v196 offset:544
	ds_write_b16_d16_hi v72, v197 offset:608
	ds_write_b16_d16_hi v72, v198 offset:672
	ds_write_b16_d16_hi v72, v199 offset:736
	ds_read_u16 v196, v72 offset:2176
	ds_read_u16 v197, v72 offset:2240
	ds_read_u16 v198, v72 offset:2304
	ds_read_u16 v199, v72 offset:2368
	s_waitcnt lgkmcnt(4)
	v_lshlrev_b32_e32 v200, 16, v200
	v_lshlrev_b32_e32 v201, 16, v201
	v_lshlrev_b32_e32 v202, 16, v202
	v_lshlrev_b32_e32 v203, 16, v203
	v_fmac_f32_e32 v200, v23, v183
	v_fmac_f32_e32 v201, v39, v183
	v_fmac_f32_e32 v202, v55, v183
	v_fmac_f32_e32 v203, v7, v183
	v_bfe_u32 v204, v200, 16, 1
	v_bfe_u32 v205, v201, 16, 1
	v_bfe_u32 v206, v202, 16, 1
	v_bfe_u32 v207, v203, 16, 1
	v_add3_u32 v200, v200, v204, s96
	v_add3_u32 v201, v201, v205, s96
	v_add3_u32 v202, v202, v206, s96
	v_add3_u32 v203, v203, v207, s96
	ds_write_b16_d16_hi v72, v200 offset:816
	ds_write_b16_d16_hi v72, v201 offset:880
	ds_write_b16_d16_hi v72, v202 offset:944
	ds_write_b16_d16_hi v72, v203 offset:1008
	ds_read_u16 v200, v72 offset:2448
	ds_read_u16 v201, v72 offset:2512
	ds_read_u16 v202, v72 offset:2576
	ds_read_u16 v203, v72 offset:2640
	s_waitcnt lgkmcnt(4)
	v_lshlrev_b32_e32 v196, 16, v196
	v_lshlrev_b32_e32 v197, 16, v197
	v_lshlrev_b32_e32 v198, 16, v198
	v_lshlrev_b32_e32 v199, 16, v199
	v_fmac_f32_e32 v196, v24, v184
	v_fmac_f32_e32 v197, v40, v184
	v_fmac_f32_e32 v198, v56, v184
	v_fmac_f32_e32 v199, v8, v184
	v_bfe_u32 v204, v196, 16, 1
	v_bfe_u32 v205, v197, 16, 1
	v_bfe_u32 v206, v198, 16, 1
	v_bfe_u32 v207, v199, 16, 1
	v_add3_u32 v196, v196, v204, s96
	v_add3_u32 v197, v197, v205, s96
	v_add3_u32 v198, v198, v206, s96
	v_add3_u32 v199, v199, v207, s96
	ds_write_b16_d16_hi v72, v196 offset:2176
	ds_write_b16_d16_hi v72, v197 offset:2240
	ds_write_b16_d16_hi v72, v198 offset:2304
	ds_write_b16_d16_hi v72, v199 offset:2368
	ds_read_u16 v196, v72 offset:2720
	ds_read_u16 v197, v72 offset:2784
	ds_read_u16 v198, v72 offset:2848
	ds_read_u16 v199, v72 offset:2912
	s_waitcnt lgkmcnt(4)
	v_lshlrev_b32_e32 v200, 16, v200
	v_lshlrev_b32_e32 v201, 16, v201
	v_lshlrev_b32_e32 v202, 16, v202
	v_lshlrev_b32_e32 v203, 16, v203
	v_fmac_f32_e32 v200, v25, v185
	v_fmac_f32_e32 v201, v41, v185
	v_fmac_f32_e32 v202, v57, v185
	v_fmac_f32_e32 v203, v9, v185
	v_bfe_u32 v204, v200, 16, 1
	v_bfe_u32 v205, v201, 16, 1
	v_bfe_u32 v206, v202, 16, 1
	v_bfe_u32 v207, v203, 16, 1
	v_add3_u32 v200, v200, v204, s96
	v_add3_u32 v201, v201, v205, s96
	v_add3_u32 v202, v202, v206, s96
	v_add3_u32 v203, v203, v207, s96
	ds_write_b16_d16_hi v72, v200 offset:2448
	ds_write_b16_d16_hi v72, v201 offset:2512
	ds_write_b16_d16_hi v72, v202 offset:2576
	ds_write_b16_d16_hi v72, v203 offset:2640
	ds_read_u16 v200, v72 offset:2992
	ds_read_u16 v201, v72 offset:3056
	ds_read_u16 v202, v72 offset:3120
	ds_read_u16 v203, v72 offset:3184
	s_waitcnt lgkmcnt(4)
	v_lshlrev_b32_e32 v196, 16, v196
	v_lshlrev_b32_e32 v197, 16, v197
	v_lshlrev_b32_e32 v198, 16, v198
	v_lshlrev_b32_e32 v199, 16, v199
	v_fmac_f32_e32 v196, v26, v186
	v_fmac_f32_e32 v197, v42, v186
	v_fmac_f32_e32 v198, v58, v186
	v_fmac_f32_e32 v199, v10, v186
	v_bfe_u32 v204, v196, 16, 1
	v_bfe_u32 v205, v197, 16, 1
	v_bfe_u32 v206, v198, 16, 1
	v_bfe_u32 v207, v199, 16, 1
	v_add3_u32 v196, v196, v204, s96
	v_add3_u32 v197, v197, v205, s96
	v_add3_u32 v198, v198, v206, s96
	v_add3_u32 v199, v199, v207, s96
	ds_write_b16_d16_hi v72, v196 offset:2720
	ds_write_b16_d16_hi v72, v197 offset:2784
	ds_write_b16_d16_hi v72, v198 offset:2848
	ds_write_b16_d16_hi v72, v199 offset:2912
	ds_read_u16 v196, v72 offset:4352
	ds_read_u16 v197, v72 offset:4416
	ds_read_u16 v198, v72 offset:4480
	ds_read_u16 v199, v72 offset:4544
	s_waitcnt lgkmcnt(4)
	v_lshlrev_b32_e32 v200, 16, v200
	v_lshlrev_b32_e32 v201, 16, v201
	v_lshlrev_b32_e32 v202, 16, v202
	v_lshlrev_b32_e32 v203, 16, v203
	v_fmac_f32_e32 v200, v27, v187
	v_fmac_f32_e32 v201, v43, v187
	v_fmac_f32_e32 v202, v59, v187
	v_fmac_f32_e32 v203, v11, v187
	v_bfe_u32 v204, v200, 16, 1
	v_bfe_u32 v205, v201, 16, 1
	v_bfe_u32 v206, v202, 16, 1
	v_bfe_u32 v207, v203, 16, 1
	v_add3_u32 v200, v200, v204, s96
	v_add3_u32 v201, v201, v205, s96
	v_add3_u32 v202, v202, v206, s96
	v_add3_u32 v203, v203, v207, s96
	ds_write_b16_d16_hi v72, v200 offset:2992
	ds_write_b16_d16_hi v72, v201 offset:3056
	ds_write_b16_d16_hi v72, v202 offset:3120
	ds_write_b16_d16_hi v72, v203 offset:3184
	ds_read_u16 v200, v72 offset:4624
	ds_read_u16 v201, v72 offset:4688
	ds_read_u16 v202, v72 offset:4752
	ds_read_u16 v203, v72 offset:4816
	s_waitcnt lgkmcnt(4)
	v_lshlrev_b32_e32 v196, 16, v196
	v_lshlrev_b32_e32 v197, 16, v197
	v_lshlrev_b32_e32 v198, 16, v198
	v_lshlrev_b32_e32 v199, 16, v199
	v_fmac_f32_e32 v196, v28, v188
	v_fmac_f32_e32 v197, v44, v188
	v_fmac_f32_e32 v198, v60, v188
	v_fmac_f32_e32 v199, v12, v188
	v_bfe_u32 v204, v196, 16, 1
	v_bfe_u32 v205, v197, 16, 1
	v_bfe_u32 v206, v198, 16, 1
	v_bfe_u32 v207, v199, 16, 1
	v_add3_u32 v196, v196, v204, s96
	v_add3_u32 v197, v197, v205, s96
	v_add3_u32 v198, v198, v206, s96
	v_add3_u32 v199, v199, v207, s96
	ds_write_b16_d16_hi v72, v196 offset:4352
	ds_write_b16_d16_hi v72, v197 offset:4416
	ds_write_b16_d16_hi v72, v198 offset:4480
	ds_write_b16_d16_hi v72, v199 offset:4544
	ds_read_u16 v196, v72 offset:4896
	ds_read_u16 v197, v72 offset:4960
	ds_read_u16 v198, v72 offset:5024
	ds_read_u16 v199, v72 offset:5088
	s_waitcnt lgkmcnt(4)
	v_lshlrev_b32_e32 v200, 16, v200
	v_lshlrev_b32_e32 v201, 16, v201
	v_lshlrev_b32_e32 v202, 16, v202
	v_lshlrev_b32_e32 v203, 16, v203
	v_fmac_f32_e32 v200, v29, v189
	v_fmac_f32_e32 v201, v45, v189
	v_fmac_f32_e32 v202, v61, v189
	v_fmac_f32_e32 v203, v13, v189
	v_bfe_u32 v204, v200, 16, 1
	v_bfe_u32 v205, v201, 16, 1
	v_bfe_u32 v206, v202, 16, 1
	v_bfe_u32 v207, v203, 16, 1
	v_add3_u32 v200, v200, v204, s96
	v_add3_u32 v201, v201, v205, s96
	v_add3_u32 v202, v202, v206, s96
	v_add3_u32 v203, v203, v207, s96
	ds_write_b16_d16_hi v72, v200 offset:4624
	ds_write_b16_d16_hi v72, v201 offset:4688
	ds_write_b16_d16_hi v72, v202 offset:4752
	ds_write_b16_d16_hi v72, v203 offset:4816
	ds_read_u16 v200, v72 offset:5168
	ds_read_u16 v201, v72 offset:5232
	ds_read_u16 v202, v72 offset:5296
	ds_read_u16 v203, v72 offset:5360
	s_waitcnt lgkmcnt(4)
	v_lshlrev_b32_e32 v196, 16, v196
	v_lshlrev_b32_e32 v197, 16, v197
	v_lshlrev_b32_e32 v198, 16, v198
	v_lshlrev_b32_e32 v199, 16, v199
	v_fmac_f32_e32 v196, v30, v190
	v_fmac_f32_e32 v197, v46, v190
	v_fmac_f32_e32 v198, v62, v190
	v_fmac_f32_e32 v199, v14, v190
	v_bfe_u32 v204, v196, 16, 1
	v_bfe_u32 v205, v197, 16, 1
	v_bfe_u32 v206, v198, 16, 1
	v_bfe_u32 v207, v199, 16, 1
	v_add3_u32 v196, v196, v204, s96
	v_add3_u32 v197, v197, v205, s96
	v_add3_u32 v198, v198, v206, s96
	v_add3_u32 v199, v199, v207, s96
	ds_write_b16_d16_hi v72, v196 offset:4896
	ds_write_b16_d16_hi v72, v197 offset:4960
	ds_write_b16_d16_hi v72, v198 offset:5024
	ds_write_b16_d16_hi v72, v199 offset:5088
	ds_read_u16 v196, v72 offset:6528
	ds_read_u16 v197, v72 offset:6592
	ds_read_u16 v198, v72 offset:6656
	ds_read_u16 v199, v72 offset:6720
	s_waitcnt lgkmcnt(4)
	v_lshlrev_b32_e32 v200, 16, v200
	v_lshlrev_b32_e32 v201, 16, v201
	v_lshlrev_b32_e32 v202, 16, v202
	v_lshlrev_b32_e32 v203, 16, v203
	v_fmac_f32_e32 v200, v31, v191
	v_fmac_f32_e32 v201, v47, v191
	v_fmac_f32_e32 v202, v63, v191
	v_fmac_f32_e32 v203, v15, v191
	v_bfe_u32 v204, v200, 16, 1
	v_bfe_u32 v205, v201, 16, 1
	v_bfe_u32 v206, v202, 16, 1
	v_bfe_u32 v207, v203, 16, 1
	v_add3_u32 v200, v200, v204, s96
	v_add3_u32 v201, v201, v205, s96
	v_add3_u32 v202, v202, v206, s96
	v_add3_u32 v203, v203, v207, s96
	ds_write_b16_d16_hi v72, v200 offset:5168
	ds_write_b16_d16_hi v72, v201 offset:5232
	ds_write_b16_d16_hi v72, v202 offset:5296
	ds_write_b16_d16_hi v72, v203 offset:5360
	ds_read_u16 v200, v72 offset:6800
	ds_read_u16 v201, v72 offset:6864
	ds_read_u16 v202, v72 offset:6928
	ds_read_u16 v203, v72 offset:6992
	s_waitcnt lgkmcnt(4)
	v_lshlrev_b32_e32 v196, 16, v196
	v_lshlrev_b32_e32 v197, 16, v197
	v_lshlrev_b32_e32 v198, 16, v198
	v_lshlrev_b32_e32 v199, 16, v199
	v_fmac_f32_e32 v196, v32, v192
	v_fmac_f32_e32 v197, v48, v192
	v_fmac_f32_e32 v198, v64, v192
	v_fmac_f32_e32 v199, v16, v192
	v_bfe_u32 v204, v196, 16, 1
	v_bfe_u32 v205, v197, 16, 1
	v_bfe_u32 v206, v198, 16, 1
	v_bfe_u32 v207, v199, 16, 1
	v_add3_u32 v196, v196, v204, s96
	v_add3_u32 v197, v197, v205, s96
	v_add3_u32 v198, v198, v206, s96
	v_add3_u32 v199, v199, v207, s96
	ds_write_b16_d16_hi v72, v196 offset:6528
	ds_write_b16_d16_hi v72, v197 offset:6592
	ds_write_b16_d16_hi v72, v198 offset:6656
	ds_write_b16_d16_hi v72, v199 offset:6720
	ds_read_u16 v196, v72 offset:7072
	ds_read_u16 v197, v72 offset:7136
	ds_read_u16 v198, v72 offset:7200
	ds_read_u16 v199, v72 offset:7264
	s_waitcnt lgkmcnt(4)
	v_lshlrev_b32_e32 v200, 16, v200
	v_lshlrev_b32_e32 v201, 16, v201
	v_lshlrev_b32_e32 v202, 16, v202
	v_lshlrev_b32_e32 v203, 16, v203
	v_fmac_f32_e32 v200, v33, v193
	v_fmac_f32_e32 v201, v49, v193
	v_fmac_f32_e32 v202, v65, v193
	v_fmac_f32_e32 v203, v17, v193
	v_bfe_u32 v204, v200, 16, 1
	v_bfe_u32 v205, v201, 16, 1
	v_bfe_u32 v206, v202, 16, 1
	v_bfe_u32 v207, v203, 16, 1
	v_add3_u32 v200, v200, v204, s96
	v_add3_u32 v201, v201, v205, s96
	v_add3_u32 v202, v202, v206, s96
	v_add3_u32 v203, v203, v207, s96
	ds_write_b16_d16_hi v72, v200 offset:6800
	ds_write_b16_d16_hi v72, v201 offset:6864
	ds_write_b16_d16_hi v72, v202 offset:6928
	ds_write_b16_d16_hi v72, v203 offset:6992
	ds_read_u16 v200, v72 offset:7344
	ds_read_u16 v201, v72 offset:7408
	ds_read_u16 v202, v72 offset:7472
	ds_read_u16 v203, v72 offset:7536
	s_waitcnt lgkmcnt(4)
	v_lshlrev_b32_e32 v196, 16, v196
	v_lshlrev_b32_e32 v197, 16, v197
	v_lshlrev_b32_e32 v198, 16, v198
	v_lshlrev_b32_e32 v199, 16, v199
	v_fmac_f32_e32 v196, v34, v194
	v_fmac_f32_e32 v197, v50, v194
	v_fmac_f32_e32 v198, v66, v194
	v_fmac_f32_e32 v199, v18, v194
	v_bfe_u32 v204, v196, 16, 1
	v_bfe_u32 v205, v197, 16, 1
	v_bfe_u32 v206, v198, 16, 1
	v_bfe_u32 v207, v199, 16, 1
	v_add3_u32 v196, v196, v204, s96
	v_add3_u32 v197, v197, v205, s96
	v_add3_u32 v198, v198, v206, s96
	v_add3_u32 v199, v199, v207, s96
	ds_write_b16_d16_hi v72, v196 offset:7072
	ds_write_b16_d16_hi v72, v197 offset:7136
	ds_write_b16_d16_hi v72, v198 offset:7200
	ds_write_b16_d16_hi v72, v199 offset:7264
	s_waitcnt lgkmcnt(4)
	v_lshlrev_b32_e32 v200, 16, v200
	v_lshlrev_b32_e32 v201, 16, v201
	v_lshlrev_b32_e32 v202, 16, v202
	v_lshlrev_b32_e32 v203, 16, v203
	v_fmac_f32_e32 v200, v35, v195
	v_fmac_f32_e32 v201, v51, v195
	v_fmac_f32_e32 v202, v67, v195
	v_fmac_f32_e32 v203, v19, v195
	v_bfe_u32 v204, v200, 16, 1
	v_bfe_u32 v205, v201, 16, 1
	v_bfe_u32 v206, v202, 16, 1
	v_bfe_u32 v207, v203, 16, 1
	v_add3_u32 v200, v200, v204, s96
	v_add3_u32 v201, v201, v205, s96
	v_add3_u32 v202, v202, v206, s96
	v_add3_u32 v203, v203, v207, s96
	ds_write_b16_d16_hi v72, v200 offset:7344
	ds_write_b16_d16_hi v72, v201 offset:7408
	ds_write_b16_d16_hi v72, v202 offset:7472
	ds_write_b16_d16_hi v72, v203 offset:7536
	v_mov_b32_e32 v0, v156
	s_waitcnt lgkmcnt(0)
	s_waitcnt vmcnt(0) lgkmcnt(0)
	s_barrier
	s_nop 0
	v_lshlrev_b32_e32 v1, 3, v0
	v_and_b32_e32 v2, 0x78, v1
	v_ashrrev_i32_e32 v1, 4, v0
	v_mad_u64_u32 v[4:5], s[4:5], v1, s1, v[2:3]
	v_lshl_add_u32 v4, v4, 1, s72
	ds_read_b128 v[4:7], v4
	v_and_or_b32 v1, v1, 3, s3
	s_waitcnt lgkmcnt(0)
	v_lshlrev_b32_e32 v8, 16, v4
	v_and_b32_e32 v4, 0xffff0000, v4
	v_mul_f32_e32 v8, 0x41800000, v8
	v_mul_f32_e32 v9, 0x41800000, v4
	v_mov_b32_e32 v4, v3
	v_cvt_pk_fp8_f32 v4, v8, v9
	v_lshlrev_b32_e32 v8, 16, v5
	v_and_b32_e32 v5, 0xffff0000, v5
	v_mul_f32_e32 v8, 0x41800000, v8
	v_mul_f32_e32 v5, 0x41800000, v5
	v_cvt_pk_fp8_f32 v4, v8, v5 op_sel:[0,0,1]
	v_lshlrev_b32_e32 v5, 16, v6
	v_mul_f32_e32 v8, 0x41800000, v5
	v_and_b32_e32 v5, 0xffff0000, v6
	v_mul_f32_e32 v6, 0x41800000, v5
	v_mov_b32_e32 v5, v3
	v_cvt_pk_fp8_f32 v5, v8, v6
	v_lshlrev_b32_e32 v6, 16, v7
	v_and_b32_e32 v7, 0xffff0000, v7
	v_mul_f32_e32 v6, 0x41800000, v6
	v_mul_f32_e32 v7, 0x41800000, v7
	v_cvt_pk_fp8_f32 v5, v6, v7 op_sel:[0,0,1]
	v_ashrrev_i32_e32 v6, 6, v0
	v_ashrrev_i32_e32 v7, 31, v6
	v_lshl_add_u64 v[6:7], s[8:9], 0, v[6:7]
	v_lshlrev_b64 v[6:7], 11, v[6:7]
	v_lshl_add_u64 v[6:7], s[6:7], 0, v[6:7]
	v_lshlrev_b32_e32 v8, 7, v1
	v_mov_b32_e32 v9, v3
	v_lshl_add_u64 v[6:7], v[6:7], 0, v[8:9]
	v_add_u32_e32 v1, 0x200, v0
	v_lshl_add_u64 v[6:7], v[6:7], 0, v[2:3]
	v_ashrrev_i32_e32 v8, 4, v1
	global_store_dwordx2 v[6:7], v[4:5], off
	v_mad_u64_u32 v[4:5], s[4:5], v8, s1, v[2:3]
	v_lshl_add_u32 v4, v4, 1, s72
	ds_read_b128 v[4:7], v4
	s_waitcnt lgkmcnt(0)
	v_lshlrev_b32_e32 v9, 16, v4
	v_and_b32_e32 v4, 0xffff0000, v4
	v_mul_f32_e32 v9, 0x41800000, v9
	v_mul_f32_e32 v10, 0x41800000, v4
	v_mov_b32_e32 v4, v3
	v_cvt_pk_fp8_f32 v4, v9, v10
	v_lshlrev_b32_e32 v9, 16, v5
	v_and_b32_e32 v5, 0xffff0000, v5
	v_mul_f32_e32 v9, 0x41800000, v9
	v_mul_f32_e32 v5, 0x41800000, v5
	v_cvt_pk_fp8_f32 v4, v9, v5 op_sel:[0,0,1]
	v_lshlrev_b32_e32 v5, 16, v6
	v_mul_f32_e32 v9, 0x41800000, v5
	v_and_b32_e32 v5, 0xffff0000, v6
	v_mul_f32_e32 v6, 0x41800000, v5
	v_mov_b32_e32 v5, v3
	v_cvt_pk_fp8_f32 v5, v9, v6
	v_lshlrev_b32_e32 v6, 16, v7
	v_and_b32_e32 v7, 0xffff0000, v7
	v_mul_f32_e32 v6, 0x41800000, v6
	v_mul_f32_e32 v7, 0x41800000, v7
	v_cvt_pk_fp8_f32 v5, v6, v7 op_sel:[0,0,1]
	v_ashrrev_i32_e32 v6, 6, v1
	v_ashrrev_i32_e32 v7, 31, v6
	v_lshl_add_u64 v[6:7], s[8:9], 0, v[6:7]
	v_lshlrev_b64 v[6:7], 11, v[6:7]
	v_and_or_b32 v1, v8, 3, s3
	v_lshl_add_u64 v[6:7], s[6:7], 0, v[6:7]
	v_lshlrev_b32_e32 v8, 7, v1
	v_mov_b32_e32 v9, v3
	v_lshl_add_u64 v[6:7], v[6:7], 0, v[8:9]
	v_add_u32_e32 v1, 0x400, v0
	v_lshl_add_u64 v[6:7], v[6:7], 0, v[2:3]
	v_ashrrev_i32_e32 v8, 4, v1
	global_store_dwordx2 v[6:7], v[4:5], off
	v_mad_u64_u32 v[4:5], s[4:5], v8, s1, v[2:3]
	v_lshl_add_u32 v4, v4, 1, s72
	ds_read_b128 v[4:7], v4
	s_waitcnt lgkmcnt(0)
	v_lshlrev_b32_e32 v9, 16, v4
	v_and_b32_e32 v4, 0xffff0000, v4
	v_mul_f32_e32 v9, 0x41800000, v9
	v_mul_f32_e32 v10, 0x41800000, v4
	v_mov_b32_e32 v4, v3
	v_cvt_pk_fp8_f32 v4, v9, v10
	v_lshlrev_b32_e32 v9, 16, v5
	v_and_b32_e32 v5, 0xffff0000, v5
	v_mul_f32_e32 v9, 0x41800000, v9
	v_mul_f32_e32 v5, 0x41800000, v5
	v_cvt_pk_fp8_f32 v4, v9, v5 op_sel:[0,0,1]
	v_lshlrev_b32_e32 v5, 16, v6
	v_mul_f32_e32 v9, 0x41800000, v5
	v_and_b32_e32 v5, 0xffff0000, v6
	v_mul_f32_e32 v6, 0x41800000, v5
	v_mov_b32_e32 v5, v3
	v_cvt_pk_fp8_f32 v5, v9, v6
	v_lshlrev_b32_e32 v6, 16, v7
	v_and_b32_e32 v7, 0xffff0000, v7
	v_mul_f32_e32 v6, 0x41800000, v6
	v_mul_f32_e32 v7, 0x41800000, v7
	v_cvt_pk_fp8_f32 v5, v6, v7 op_sel:[0,0,1]
	v_ashrrev_i32_e32 v6, 6, v1
	v_ashrrev_i32_e32 v7, 31, v6
	v_lshl_add_u64 v[6:7], s[8:9], 0, v[6:7]
	v_lshlrev_b64 v[6:7], 11, v[6:7]
	v_and_or_b32 v1, v8, 3, s3
	v_lshl_add_u64 v[6:7], s[6:7], 0, v[6:7]
	v_lshlrev_b32_e32 v8, 7, v1
	v_mov_b32_e32 v9, v3
	v_lshl_add_u64 v[6:7], v[6:7], 0, v[8:9]
	v_add_u32_e32 v1, 0x600, v0
	v_lshl_add_u64 v[6:7], v[6:7], 0, v[2:3]
	v_ashrrev_i32_e32 v8, 4, v1
	global_store_dwordx2 v[6:7], v[4:5], off
	v_mad_u64_u32 v[4:5], s[4:5], v8, s1, v[2:3]
	v_lshl_add_u32 v4, v4, 1, s72
	ds_read_b128 v[4:7], v4
	s_waitcnt lgkmcnt(0)
	v_lshlrev_b32_e32 v9, 16, v4
	v_and_b32_e32 v4, 0xffff0000, v4
	v_mul_f32_e32 v9, 0x41800000, v9
	v_mul_f32_e32 v10, 0x41800000, v4
	v_mov_b32_e32 v4, v3
	v_cvt_pk_fp8_f32 v4, v9, v10
	v_lshlrev_b32_e32 v9, 16, v5
	v_and_b32_e32 v5, 0xffff0000, v5
	v_mul_f32_e32 v9, 0x41800000, v9
	v_mul_f32_e32 v5, 0x41800000, v5
	v_cvt_pk_fp8_f32 v4, v9, v5 op_sel:[0,0,1]
	v_lshlrev_b32_e32 v5, 16, v6
	v_mul_f32_e32 v9, 0x41800000, v5
	v_and_b32_e32 v5, 0xffff0000, v6
	v_mul_f32_e32 v6, 0x41800000, v5
	v_mov_b32_e32 v5, v3
	v_cvt_pk_fp8_f32 v5, v9, v6
	v_lshlrev_b32_e32 v6, 16, v7
	v_and_b32_e32 v7, 0xffff0000, v7
	v_mul_f32_e32 v6, 0x41800000, v6
	v_mul_f32_e32 v7, 0x41800000, v7
	v_cvt_pk_fp8_f32 v5, v6, v7 op_sel:[0,0,1]
	v_ashrrev_i32_e32 v6, 6, v1
	v_ashrrev_i32_e32 v7, 31, v6
	v_lshl_add_u64 v[6:7], s[8:9], 0, v[6:7]
	v_lshlrev_b64 v[6:7], 11, v[6:7]
	v_and_or_b32 v1, v8, 3, s3
	v_lshl_add_u64 v[6:7], s[6:7], 0, v[6:7]
	v_lshlrev_b32_e32 v8, 7, v1
	v_mov_b32_e32 v9, v3
	v_lshl_add_u64 v[6:7], v[6:7], 0, v[8:9]
	v_add_u32_e32 v1, 0x800, v0
	v_lshl_add_u64 v[6:7], v[6:7], 0, v[2:3]
	v_ashrrev_i32_e32 v8, 4, v1
	global_store_dwordx2 v[6:7], v[4:5], off
	v_mad_u64_u32 v[4:5], s[4:5], v8, s1, v[2:3]
	v_lshl_add_u32 v4, v4, 1, s72
	ds_read_b128 v[4:7], v4
	s_waitcnt lgkmcnt(0)
	v_lshlrev_b32_e32 v9, 16, v4
	v_and_b32_e32 v4, 0xffff0000, v4
	v_mul_f32_e32 v9, 0x41800000, v9
	v_mul_f32_e32 v10, 0x41800000, v4
	v_mov_b32_e32 v4, v3
	v_cvt_pk_fp8_f32 v4, v9, v10
	v_lshlrev_b32_e32 v9, 16, v5
	v_and_b32_e32 v5, 0xffff0000, v5
	v_mul_f32_e32 v9, 0x41800000, v9
	v_mul_f32_e32 v5, 0x41800000, v5
	v_cvt_pk_fp8_f32 v4, v9, v5 op_sel:[0,0,1]
	v_lshlrev_b32_e32 v5, 16, v6
	v_mul_f32_e32 v9, 0x41800000, v5
	v_and_b32_e32 v5, 0xffff0000, v6
	v_mul_f32_e32 v6, 0x41800000, v5
	v_mov_b32_e32 v5, v3
	v_cvt_pk_fp8_f32 v5, v9, v6
	v_lshlrev_b32_e32 v6, 16, v7
	v_and_b32_e32 v7, 0xffff0000, v7
	v_mul_f32_e32 v6, 0x41800000, v6
	v_mul_f32_e32 v7, 0x41800000, v7
	v_cvt_pk_fp8_f32 v5, v6, v7 op_sel:[0,0,1]
	v_ashrrev_i32_e32 v6, 6, v1
	v_ashrrev_i32_e32 v7, 31, v6
	v_lshl_add_u64 v[6:7], s[8:9], 0, v[6:7]
	v_lshlrev_b64 v[6:7], 11, v[6:7]
	v_and_or_b32 v1, v8, 3, s3
	v_lshl_add_u64 v[6:7], s[6:7], 0, v[6:7]
	v_lshlrev_b32_e32 v8, 7, v1
	v_mov_b32_e32 v9, v3
	v_lshl_add_u64 v[6:7], v[6:7], 0, v[8:9]
	v_add_u32_e32 v1, 0xa00, v0
	v_lshl_add_u64 v[6:7], v[6:7], 0, v[2:3]
	v_ashrrev_i32_e32 v8, 4, v1
	global_store_dwordx2 v[6:7], v[4:5], off
	v_mad_u64_u32 v[4:5], s[4:5], v8, s1, v[2:3]
	v_lshl_add_u32 v4, v4, 1, s72
	ds_read_b128 v[4:7], v4
	s_waitcnt lgkmcnt(0)
	v_lshlrev_b32_e32 v9, 16, v4
	v_and_b32_e32 v4, 0xffff0000, v4
	v_mul_f32_e32 v9, 0x41800000, v9
	v_mul_f32_e32 v10, 0x41800000, v4
	v_mov_b32_e32 v4, v3
	v_cvt_pk_fp8_f32 v4, v9, v10
	v_lshlrev_b32_e32 v9, 16, v5
	v_and_b32_e32 v5, 0xffff0000, v5
	v_mul_f32_e32 v9, 0x41800000, v9
	v_mul_f32_e32 v5, 0x41800000, v5
	v_cvt_pk_fp8_f32 v4, v9, v5 op_sel:[0,0,1]
	v_lshlrev_b32_e32 v5, 16, v6
	v_mul_f32_e32 v9, 0x41800000, v5
	v_and_b32_e32 v5, 0xffff0000, v6
	v_mul_f32_e32 v6, 0x41800000, v5
	v_mov_b32_e32 v5, v3
	v_cvt_pk_fp8_f32 v5, v9, v6
	v_lshlrev_b32_e32 v6, 16, v7
	v_and_b32_e32 v7, 0xffff0000, v7
	v_mul_f32_e32 v6, 0x41800000, v6
	v_mul_f32_e32 v7, 0x41800000, v7
	v_cvt_pk_fp8_f32 v5, v6, v7 op_sel:[0,0,1]
	v_ashrrev_i32_e32 v6, 6, v1
	v_ashrrev_i32_e32 v7, 31, v6
	v_lshl_add_u64 v[6:7], s[8:9], 0, v[6:7]
	v_lshlrev_b64 v[6:7], 11, v[6:7]
	v_and_or_b32 v1, v8, 3, s3
	v_lshl_add_u64 v[6:7], s[6:7], 0, v[6:7]
	v_lshlrev_b32_e32 v8, 7, v1
	v_mov_b32_e32 v9, v3
	v_lshl_add_u64 v[6:7], v[6:7], 0, v[8:9]
	v_add_u32_e32 v1, 0xc00, v0
	v_lshl_add_u64 v[6:7], v[6:7], 0, v[2:3]
	v_ashrrev_i32_e32 v8, 4, v1
	global_store_dwordx2 v[6:7], v[4:5], off
	v_mad_u64_u32 v[4:5], s[4:5], v8, s1, v[2:3]
	v_lshl_add_u32 v4, v4, 1, s72
	ds_read_b128 v[4:7], v4
	s_waitcnt lgkmcnt(0)
	v_lshlrev_b32_e32 v9, 16, v4
	v_and_b32_e32 v4, 0xffff0000, v4
	v_mul_f32_e32 v9, 0x41800000, v9
	v_mul_f32_e32 v10, 0x41800000, v4
	v_mov_b32_e32 v4, v3
	v_cvt_pk_fp8_f32 v4, v9, v10
	v_lshlrev_b32_e32 v9, 16, v5
	v_and_b32_e32 v5, 0xffff0000, v5
	v_mul_f32_e32 v9, 0x41800000, v9
	v_mul_f32_e32 v5, 0x41800000, v5
	v_cvt_pk_fp8_f32 v4, v9, v5 op_sel:[0,0,1]
	v_lshlrev_b32_e32 v5, 16, v6
	v_mul_f32_e32 v9, 0x41800000, v5
	v_and_b32_e32 v5, 0xffff0000, v6
	v_mul_f32_e32 v6, 0x41800000, v5
	v_mov_b32_e32 v5, v3
	v_cvt_pk_fp8_f32 v5, v9, v6
	v_lshlrev_b32_e32 v6, 16, v7
	v_and_b32_e32 v7, 0xffff0000, v7
	v_mul_f32_e32 v6, 0x41800000, v6
	v_mul_f32_e32 v7, 0x41800000, v7
	v_cvt_pk_fp8_f32 v5, v6, v7 op_sel:[0,0,1]
	v_ashrrev_i32_e32 v6, 6, v1
	v_ashrrev_i32_e32 v7, 31, v6
	v_lshl_add_u64 v[6:7], s[8:9], 0, v[6:7]
	v_lshlrev_b64 v[6:7], 11, v[6:7]
	v_and_or_b32 v1, v8, 3, s3
	v_lshl_add_u64 v[6:7], s[6:7], 0, v[6:7]
	v_lshlrev_b32_e32 v8, 7, v1
	v_mov_b32_e32 v9, v3
	v_lshl_add_u64 v[6:7], v[6:7], 0, v[8:9]
	v_add_u32_e32 v8, 0xe00, v0
	v_ashrrev_i32_e32 v9, 4, v8
	v_mad_u64_u32 v[0:1], s[4:5], v9, s1, v[2:3]
	v_lshl_add_u64 v[6:7], v[6:7], 0, v[2:3]
	v_lshl_add_u32 v0, v0, 1, s72
	global_store_dwordx2 v[6:7], v[4:5], off
	ds_read_b128 v[4:7], v0
	v_readlane_b32 s4, v255, 7
	v_readlane_b32 s5, v255, 8
	s_and_b64 s[4:5], s[4:5], exec
	v_readlane_b32 s1, v254, 38
	s_waitcnt lgkmcnt(0)
	v_lshlrev_b32_e32 v0, 16, v4
	v_mul_f32_e32 v1, 0x41800000, v0
	v_and_b32_e32 v0, 0xffff0000, v4
	v_mul_f32_e32 v4, 0x41800000, v0
	v_mov_b32_e32 v0, v3
	v_cvt_pk_fp8_f32 v0, v1, v4
	v_lshlrev_b32_e32 v1, 16, v5
	v_and_b32_e32 v4, 0xffff0000, v5
	v_mul_f32_e32 v1, 0x41800000, v1
	v_mul_f32_e32 v4, 0x41800000, v4
	v_cvt_pk_fp8_f32 v0, v1, v4 op_sel:[0,0,1]
	v_lshlrev_b32_e32 v1, 16, v6
	v_mul_f32_e32 v4, 0x41800000, v1
	v_and_b32_e32 v1, 0xffff0000, v6
	v_mul_f32_e32 v5, 0x41800000, v1
	v_mov_b32_e32 v1, v3
	v_cvt_pk_fp8_f32 v1, v4, v5
	v_lshlrev_b32_e32 v4, 16, v7
	v_and_b32_e32 v5, 0xffff0000, v7
	v_mul_f32_e32 v4, 0x41800000, v4
	v_mul_f32_e32 v5, 0x41800000, v5
	v_cvt_pk_fp8_f32 v1, v4, v5 op_sel:[0,0,1]
	v_ashrrev_i32_e32 v4, 6, v8
	v_ashrrev_i32_e32 v5, 31, v4
	v_lshl_add_u64 v[4:5], s[8:9], 0, v[4:5]
	v_lshlrev_b64 v[4:5], 11, v[4:5]
	v_and_or_b32 v6, v9, 3, s3
	v_lshl_add_u64 v[4:5], s[6:7], 0, v[4:5]
	v_lshlrev_b32_e32 v6, 7, v6
	v_mov_b32_e32 v7, v3
	s_cselect_b32 s1, 1, s1
	v_readlane_b32 s5, v255, 6
	v_lshl_add_u64 v[4:5], v[4:5], 0, v[6:7]
	s_add_i32 s5, s1, s5
	v_lshl_add_u64 v[4:5], v[4:5], 0, v[2:3]
	s_cmpk_lt_i32 s5, 0x400
	global_store_dwordx2 v[4:5], v[0:1], off
	s_barrier
	s_cbranch_scc0 .LBB0_2104

.LBB0_1912:
	s_or_b64 exec, exec, s[8:9]
	v_mov_b32_e32 v1, v156
	s_nop 0
	v_bfe_u32 v69, v1, 5, 1
	v_and_b32_e32 v68, 31, v1
	v_cmp_eq_u32_e32 vcc, 0, v69
	s_and_saveexec_b64 s[4:5], vcc
	v_lshl_add_u32 v1, v68, 2, s45
	ds_write_b32 v1, v0
	s_or_b64 exec, exec, s[4:5]
	v_lshlrev_b32_e32 v1, 2, v69
	v_lshl_add_u32 v0, v68, 1, s72
	v_or_b32_e32 v73, s48, v1
	s_waitcnt lgkmcnt(0)
	v_lshl_add_u32 v72, v69, 4, s45
	v_mad_u64_u32 v[74:75], s[4:5], v73, s71, v[0:1]
	v_writelane_b32 v255, s52, 16
	s_sub_i32 s91, s89, s79
	s_mov_b64 s[8:9], -1
	v_writelane_b32 v255, s53, 17
	v_writelane_b32 v255, s54, 18
	v_writelane_b32 v255, s55, 19
	s_and_b64 vcc, exec, s[50:51]
	v_writelane_b32 v255, s72, 20
	ds_read_b128 v[180:183], v72
	ds_read_b128 v[184:187], v72 offset:32
	ds_read_b128 v[188:191], v72 offset:64
	ds_read_b128 v[192:195], v72 offset:96
	ds_read_u16 v196, v74 offset:0
	ds_read_u16 v197, v74 offset:64
	ds_read_u16 v198, v74 offset:128
	ds_read_u16 v199, v74 offset:192
	ds_read_u16 v200, v74 offset:272
	ds_read_u16 v201, v74 offset:336
	ds_read_u16 v202, v74 offset:400
	ds_read_u16 v203, v74 offset:464
	s_waitcnt lgkmcnt(4)
	v_lshlrev_b32_e32 v196, 16, v196
	v_lshlrev_b32_e32 v197, 16, v197
	v_lshlrev_b32_e32 v198, 16, v198
	v_lshlrev_b32_e32 v199, 16, v199
	v_fmac_f32_e32 v196, v20, v180
	v_fmac_f32_e32 v197, v36, v180
	v_fmac_f32_e32 v198, v52, v180
	v_fmac_f32_e32 v199, v4, v180
	v_bfe_u32 v204, v196, 16, 1
	v_bfe_u32 v205, v197, 16, 1
	v_bfe_u32 v206, v198, 16, 1
	v_bfe_u32 v207, v199, 16, 1
	v_add3_u32 v196, v196, v204, s96
	v_add3_u32 v197, v197, v205, s96
	v_add3_u32 v198, v198, v206, s96
	v_add3_u32 v199, v199, v207, s96
	ds_write_b16_d16_hi v74, v196 offset:0
	ds_write_b16_d16_hi v74, v197 offset:64
	ds_write_b16_d16_hi v74, v198 offset:128
	ds_write_b16_d16_hi v74, v199 offset:192
	ds_read_u16 v196, v74 offset:544
	ds_read_u16 v197, v74 offset:608
	ds_read_u16 v198, v74 offset:672
	ds_read_u16 v199, v74 offset:736
	s_waitcnt lgkmcnt(4)
	v_lshlrev_b32_e32 v200, 16, v200
	v_lshlrev_b32_e32 v201, 16, v201
	v_lshlrev_b32_e32 v202, 16, v202
	v_lshlrev_b32_e32 v203, 16, v203
	v_fmac_f32_e32 v200, v21, v181
	v_fmac_f32_e32 v201, v37, v181
	v_fmac_f32_e32 v202, v53, v181
	v_fmac_f32_e32 v203, v5, v181
	v_bfe_u32 v204, v200, 16, 1
	v_bfe_u32 v205, v201, 16, 1
	v_bfe_u32 v206, v202, 16, 1
	v_bfe_u32 v207, v203, 16, 1
	v_add3_u32 v200, v200, v204, s96
	v_add3_u32 v201, v201, v205, s96
	v_add3_u32 v202, v202, v206, s96
	v_add3_u32 v203, v203, v207, s96
	ds_write_b16_d16_hi v74, v200 offset:272
	ds_write_b16_d16_hi v74, v201 offset:336
	ds_write_b16_d16_hi v74, v202 offset:400
	ds_write_b16_d16_hi v74, v203 offset:464
	ds_read_u16 v200, v74 offset:816
	ds_read_u16 v201, v74 offset:880
	ds_read_u16 v202, v74 offset:944
	ds_read_u16 v203, v74 offset:1008
	s_waitcnt lgkmcnt(4)
	v_lshlrev_b32_e32 v196, 16, v196
	v_lshlrev_b32_e32 v197, 16, v197
	v_lshlrev_b32_e32 v198, 16, v198
	v_lshlrev_b32_e32 v199, 16, v199
	v_fmac_f32_e32 v196, v22, v182
	v_fmac_f32_e32 v197, v38, v182
	v_fmac_f32_e32 v198, v54, v182
	v_fmac_f32_e32 v199, v6, v182
	v_bfe_u32 v204, v196, 16, 1
	v_bfe_u32 v205, v197, 16, 1
	v_bfe_u32 v206, v198, 16, 1
	v_bfe_u32 v207, v199, 16, 1
	v_add3_u32 v196, v196, v204, s96
	v_add3_u32 v197, v197, v205, s96
	v_add3_u32 v198, v198, v206, s96
	v_add3_u32 v199, v199, v207, s96
	ds_write_b16_d16_hi v74, v196 offset:544
	ds_write_b16_d16_hi v74, v197 offset:608
	ds_write_b16_d16_hi v74, v198 offset:672
	ds_write_b16_d16_hi v74, v199 offset:736
	ds_read_u16 v196, v74 offset:2176
	ds_read_u16 v197, v74 offset:2240
	ds_read_u16 v198, v74 offset:2304
	ds_read_u16 v199, v74 offset:2368
	s_waitcnt lgkmcnt(4)
	v_lshlrev_b32_e32 v200, 16, v200
	v_lshlrev_b32_e32 v201, 16, v201
	v_lshlrev_b32_e32 v202, 16, v202
	v_lshlrev_b32_e32 v203, 16, v203
	v_fmac_f32_e32 v200, v23, v183
	v_fmac_f32_e32 v201, v39, v183
	v_fmac_f32_e32 v202, v55, v183
	v_fmac_f32_e32 v203, v7, v183
	v_bfe_u32 v204, v200, 16, 1
	v_bfe_u32 v205, v201, 16, 1
	v_bfe_u32 v206, v202, 16, 1
	v_bfe_u32 v207, v203, 16, 1
	v_add3_u32 v200, v200, v204, s96
	v_add3_u32 v201, v201, v205, s96
	v_add3_u32 v202, v202, v206, s96
	v_add3_u32 v203, v203, v207, s96
	ds_write_b16_d16_hi v74, v200 offset:816
	ds_write_b16_d16_hi v74, v201 offset:880
	ds_write_b16_d16_hi v74, v202 offset:944
	ds_write_b16_d16_hi v74, v203 offset:1008
	ds_read_u16 v200, v74 offset:2448
	ds_read_u16 v201, v74 offset:2512
	ds_read_u16 v202, v74 offset:2576
	ds_read_u16 v203, v74 offset:2640
	s_waitcnt lgkmcnt(4)
	v_lshlrev_b32_e32 v196, 16, v196
	v_lshlrev_b32_e32 v197, 16, v197
	v_lshlrev_b32_e32 v198, 16, v198
	v_lshlrev_b32_e32 v199, 16, v199
	v_fmac_f32_e32 v196, v24, v184
	v_fmac_f32_e32 v197, v40, v184
	v_fmac_f32_e32 v198, v56, v184
	v_fmac_f32_e32 v199, v8, v184
	v_bfe_u32 v204, v196, 16, 1
	v_bfe_u32 v205, v197, 16, 1
	v_bfe_u32 v206, v198, 16, 1
	v_bfe_u32 v207, v199, 16, 1
	v_add3_u32 v196, v196, v204, s96
	v_add3_u32 v197, v197, v205, s96
	v_add3_u32 v198, v198, v206, s96
	v_add3_u32 v199, v199, v207, s96
	ds_write_b16_d16_hi v74, v196 offset:2176
	ds_write_b16_d16_hi v74, v197 offset:2240
	ds_write_b16_d16_hi v74, v198 offset:2304
	ds_write_b16_d16_hi v74, v199 offset:2368
	ds_read_u16 v196, v74 offset:2720
	ds_read_u16 v197, v74 offset:2784
	ds_read_u16 v198, v74 offset:2848
	ds_read_u16 v199, v74 offset:2912
	s_waitcnt lgkmcnt(4)
	v_lshlrev_b32_e32 v200, 16, v200
	v_lshlrev_b32_e32 v201, 16, v201
	v_lshlrev_b32_e32 v202, 16, v202
	v_lshlrev_b32_e32 v203, 16, v203
	v_fmac_f32_e32 v200, v25, v185
	v_fmac_f32_e32 v201, v41, v185
	v_fmac_f32_e32 v202, v57, v185
	v_fmac_f32_e32 v203, v9, v185
	v_bfe_u32 v204, v200, 16, 1
	v_bfe_u32 v205, v201, 16, 1
	v_bfe_u32 v206, v202, 16, 1
	v_bfe_u32 v207, v203, 16, 1
	v_add3_u32 v200, v200, v204, s96
	v_add3_u32 v201, v201, v205, s96
	v_add3_u32 v202, v202, v206, s96
	v_add3_u32 v203, v203, v207, s96
	ds_write_b16_d16_hi v74, v200 offset:2448
	ds_write_b16_d16_hi v74, v201 offset:2512
	ds_write_b16_d16_hi v74, v202 offset:2576
	ds_write_b16_d16_hi v74, v203 offset:2640
	ds_read_u16 v200, v74 offset:2992
	ds_read_u16 v201, v74 offset:3056
	ds_read_u16 v202, v74 offset:3120
	ds_read_u16 v203, v74 offset:3184
	s_waitcnt lgkmcnt(4)
	v_lshlrev_b32_e32 v196, 16, v196
	v_lshlrev_b32_e32 v197, 16, v197
	v_lshlrev_b32_e32 v198, 16, v198
	v_lshlrev_b32_e32 v199, 16, v199
	v_fmac_f32_e32 v196, v26, v186
	v_fmac_f32_e32 v197, v42, v186
	v_fmac_f32_e32 v198, v58, v186
	v_fmac_f32_e32 v199, v10, v186
	v_bfe_u32 v204, v196, 16, 1
	v_bfe_u32 v205, v197, 16, 1
	v_bfe_u32 v206, v198, 16, 1
	v_bfe_u32 v207, v199, 16, 1
	v_add3_u32 v196, v196, v204, s96
	v_add3_u32 v197, v197, v205, s96
	v_add3_u32 v198, v198, v206, s96
	v_add3_u32 v199, v199, v207, s96
	ds_write_b16_d16_hi v74, v196 offset:2720
	ds_write_b16_d16_hi v74, v197 offset:2784
	ds_write_b16_d16_hi v74, v198 offset:2848
	ds_write_b16_d16_hi v74, v199 offset:2912
	ds_read_u16 v196, v74 offset:4352
	ds_read_u16 v197, v74 offset:4416
	ds_read_u16 v198, v74 offset:4480
	ds_read_u16 v199, v74 offset:4544
	s_waitcnt lgkmcnt(4)
	v_lshlrev_b32_e32 v200, 16, v200
	v_lshlrev_b32_e32 v201, 16, v201
	v_lshlrev_b32_e32 v202, 16, v202
	v_lshlrev_b32_e32 v203, 16, v203
	v_fmac_f32_e32 v200, v27, v187
	v_fmac_f32_e32 v201, v43, v187
	v_fmac_f32_e32 v202, v59, v187
	v_fmac_f32_e32 v203, v11, v187
	v_bfe_u32 v204, v200, 16, 1
	v_bfe_u32 v205, v201, 16, 1
	v_bfe_u32 v206, v202, 16, 1
	v_bfe_u32 v207, v203, 16, 1
	v_add3_u32 v200, v200, v204, s96
	v_add3_u32 v201, v201, v205, s96
	v_add3_u32 v202, v202, v206, s96
	v_add3_u32 v203, v203, v207, s96
	ds_write_b16_d16_hi v74, v200 offset:2992
	ds_write_b16_d16_hi v74, v201 offset:3056
	ds_write_b16_d16_hi v74, v202 offset:3120
	ds_write_b16_d16_hi v74, v203 offset:3184
	ds_read_u16 v200, v74 offset:4624
	ds_read_u16 v201, v74 offset:4688
	ds_read_u16 v202, v74 offset:4752
	ds_read_u16 v203, v74 offset:4816
	s_waitcnt lgkmcnt(4)
	v_lshlrev_b32_e32 v196, 16, v196
	v_lshlrev_b32_e32 v197, 16, v197
	v_lshlrev_b32_e32 v198, 16, v198
	v_lshlrev_b32_e32 v199, 16, v199
	v_fmac_f32_e32 v196, v28, v188
	v_fmac_f32_e32 v197, v44, v188
	v_fmac_f32_e32 v198, v60, v188
	v_fmac_f32_e32 v199, v12, v188
	v_bfe_u32 v204, v196, 16, 1
	v_bfe_u32 v205, v197, 16, 1
	v_bfe_u32 v206, v198, 16, 1
	v_bfe_u32 v207, v199, 16, 1
	v_add3_u32 v196, v196, v204, s96
	v_add3_u32 v197, v197, v205, s96
	v_add3_u32 v198, v198, v206, s96
	v_add3_u32 v199, v199, v207, s96
	ds_write_b16_d16_hi v74, v196 offset:4352
	ds_write_b16_d16_hi v74, v197 offset:4416
	ds_write_b16_d16_hi v74, v198 offset:4480
	ds_write_b16_d16_hi v74, v199 offset:4544
	ds_read_u16 v196, v74 offset:4896
	ds_read_u16 v197, v74 offset:4960
	ds_read_u16 v198, v74 offset:5024
	ds_read_u16 v199, v74 offset:5088
	s_waitcnt lgkmcnt(4)
	v_lshlrev_b32_e32 v200, 16, v200
	v_lshlrev_b32_e32 v201, 16, v201
	v_lshlrev_b32_e32 v202, 16, v202
	v_lshlrev_b32_e32 v203, 16, v203
	v_fmac_f32_e32 v200, v29, v189
	v_fmac_f32_e32 v201, v45, v189
	v_fmac_f32_e32 v202, v61, v189
	v_fmac_f32_e32 v203, v13, v189
	v_bfe_u32 v204, v200, 16, 1
	v_bfe_u32 v205, v201, 16, 1
	v_bfe_u32 v206, v202, 16, 1
	v_bfe_u32 v207, v203, 16, 1
	v_add3_u32 v200, v200, v204, s96
	v_add3_u32 v201, v201, v205, s96
	v_add3_u32 v202, v202, v206, s96
	v_add3_u32 v203, v203, v207, s96
	ds_write_b16_d16_hi v74, v200 offset:4624
	ds_write_b16_d16_hi v74, v201 offset:4688
	ds_write_b16_d16_hi v74, v202 offset:4752
	ds_write_b16_d16_hi v74, v203 offset:4816
	ds_read_u16 v200, v74 offset:5168
	ds_read_u16 v201, v74 offset:5232
	ds_read_u16 v202, v74 offset:5296
	ds_read_u16 v203, v74 offset:5360
	s_waitcnt lgkmcnt(4)
	v_lshlrev_b32_e32 v196, 16, v196
	v_lshlrev_b32_e32 v197, 16, v197
	v_lshlrev_b32_e32 v198, 16, v198
	v_lshlrev_b32_e32 v199, 16, v199
	v_fmac_f32_e32 v196, v30, v190
	v_fmac_f32_e32 v197, v46, v190
	v_fmac_f32_e32 v198, v62, v190
	v_fmac_f32_e32 v199, v14, v190
	v_bfe_u32 v204, v196, 16, 1
	v_bfe_u32 v205, v197, 16, 1
	v_bfe_u32 v206, v198, 16, 1
	v_bfe_u32 v207, v199, 16, 1
	v_add3_u32 v196, v196, v204, s96
	v_add3_u32 v197, v197, v205, s96
	v_add3_u32 v198, v198, v206, s96
	v_add3_u32 v199, v199, v207, s96
	ds_write_b16_d16_hi v74, v196 offset:4896
	ds_write_b16_d16_hi v74, v197 offset:4960
	ds_write_b16_d16_hi v74, v198 offset:5024
	ds_write_b16_d16_hi v74, v199 offset:5088
	ds_read_u16 v196, v74 offset:6528
	ds_read_u16 v197, v74 offset:6592
	ds_read_u16 v198, v74 offset:6656
	ds_read_u16 v199, v74 offset:6720
	s_waitcnt lgkmcnt(4)
	v_lshlrev_b32_e32 v200, 16, v200
	v_lshlrev_b32_e32 v201, 16, v201
	v_lshlrev_b32_e32 v202, 16, v202
	v_lshlrev_b32_e32 v203, 16, v203
	v_fmac_f32_e32 v200, v31, v191
	v_fmac_f32_e32 v201, v47, v191
	v_fmac_f32_e32 v202, v63, v191
	v_fmac_f32_e32 v203, v15, v191
	v_bfe_u32 v204, v200, 16, 1
	v_bfe_u32 v205, v201, 16, 1
	v_bfe_u32 v206, v202, 16, 1
	v_bfe_u32 v207, v203, 16, 1
	v_add3_u32 v200, v200, v204, s96
	v_add3_u32 v201, v201, v205, s96
	v_add3_u32 v202, v202, v206, s96
	v_add3_u32 v203, v203, v207, s96
	ds_write_b16_d16_hi v74, v200 offset:5168
	ds_write_b16_d16_hi v74, v201 offset:5232
	ds_write_b16_d16_hi v74, v202 offset:5296
	ds_write_b16_d16_hi v74, v203 offset:5360
	ds_read_u16 v200, v74 offset:6800
	ds_read_u16 v201, v74 offset:6864
	ds_read_u16 v202, v74 offset:6928
	ds_read_u16 v203, v74 offset:6992
	s_waitcnt lgkmcnt(4)
	v_lshlrev_b32_e32 v196, 16, v196
	v_lshlrev_b32_e32 v197, 16, v197
	v_lshlrev_b32_e32 v198, 16, v198
	v_lshlrev_b32_e32 v199, 16, v199
	v_fmac_f32_e32 v196, v32, v192
	v_fmac_f32_e32 v197, v48, v192
	v_fmac_f32_e32 v198, v64, v192
	v_fmac_f32_e32 v199, v16, v192
	v_bfe_u32 v204, v196, 16, 1
	v_bfe_u32 v205, v197, 16, 1
	v_bfe_u32 v206, v198, 16, 1
	v_bfe_u32 v207, v199, 16, 1
	v_add3_u32 v196, v196, v204, s96
	v_add3_u32 v197, v197, v205, s96
	v_add3_u32 v198, v198, v206, s96
	v_add3_u32 v199, v199, v207, s96
	ds_write_b16_d16_hi v74, v196 offset:6528
	ds_write_b16_d16_hi v74, v197 offset:6592
	ds_write_b16_d16_hi v74, v198 offset:6656
	ds_write_b16_d16_hi v74, v199 offset:6720
	ds_read_u16 v196, v74 offset:7072
	ds_read_u16 v197, v74 offset:7136
	ds_read_u16 v198, v74 offset:7200
	ds_read_u16 v199, v74 offset:7264
	s_waitcnt lgkmcnt(4)
	v_lshlrev_b32_e32 v200, 16, v200
	v_lshlrev_b32_e32 v201, 16, v201
	v_lshlrev_b32_e32 v202, 16, v202
	v_lshlrev_b32_e32 v203, 16, v203
	v_fmac_f32_e32 v200, v33, v193
	v_fmac_f32_e32 v201, v49, v193
	v_fmac_f32_e32 v202, v65, v193
	v_fmac_f32_e32 v203, v17, v193
	v_bfe_u32 v204, v200, 16, 1
	v_bfe_u32 v205, v201, 16, 1
	v_bfe_u32 v206, v202, 16, 1
	v_bfe_u32 v207, v203, 16, 1
	v_add3_u32 v200, v200, v204, s96
	v_add3_u32 v201, v201, v205, s96
	v_add3_u32 v202, v202, v206, s96
	v_add3_u32 v203, v203, v207, s96
	ds_write_b16_d16_hi v74, v200 offset:6800
	ds_write_b16_d16_hi v74, v201 offset:6864
	ds_write_b16_d16_hi v74, v202 offset:6928
	ds_write_b16_d16_hi v74, v203 offset:6992
	ds_read_u16 v200, v74 offset:7344
	ds_read_u16 v201, v74 offset:7408
	ds_read_u16 v202, v74 offset:7472
	ds_read_u16 v203, v74 offset:7536
	s_waitcnt lgkmcnt(4)
	v_lshlrev_b32_e32 v196, 16, v196
	v_lshlrev_b32_e32 v197, 16, v197
	v_lshlrev_b32_e32 v198, 16, v198
	v_lshlrev_b32_e32 v199, 16, v199
	v_fmac_f32_e32 v196, v34, v194
	v_fmac_f32_e32 v197, v50, v194
	v_fmac_f32_e32 v198, v66, v194
	v_fmac_f32_e32 v199, v18, v194
	v_bfe_u32 v204, v196, 16, 1
	v_bfe_u32 v205, v197, 16, 1
	v_bfe_u32 v206, v198, 16, 1
	v_bfe_u32 v207, v199, 16, 1
	v_add3_u32 v196, v196, v204, s96
	v_add3_u32 v197, v197, v205, s96
	v_add3_u32 v198, v198, v206, s96
	v_add3_u32 v199, v199, v207, s96
	ds_write_b16_d16_hi v74, v196 offset:7072
	ds_write_b16_d16_hi v74, v197 offset:7136
	ds_write_b16_d16_hi v74, v198 offset:7200
	ds_write_b16_d16_hi v74, v199 offset:7264
	s_waitcnt lgkmcnt(4)
	v_lshlrev_b32_e32 v200, 16, v200
	v_lshlrev_b32_e32 v201, 16, v201
	v_lshlrev_b32_e32 v202, 16, v202
	v_lshlrev_b32_e32 v203, 16, v203
	v_fmac_f32_e32 v200, v35, v195
	v_fmac_f32_e32 v201, v51, v195
	v_fmac_f32_e32 v202, v67, v195
	v_fmac_f32_e32 v203, v19, v195
	v_bfe_u32 v204, v200, 16, 1
	v_bfe_u32 v205, v201, 16, 1
	v_bfe_u32 v206, v202, 16, 1
	v_bfe_u32 v207, v203, 16, 1
	v_add3_u32 v200, v200, v204, s96
	v_add3_u32 v201, v201, v205, s96
	v_add3_u32 v202, v202, v206, s96
	v_add3_u32 v203, v203, v207, s96
	ds_write_b16_d16_hi v74, v200 offset:7344
	ds_write_b16_d16_hi v74, v201 offset:7408
	ds_write_b16_d16_hi v74, v202 offset:7472
	ds_write_b16_d16_hi v74, v203 offset:7536
	s_waitcnt lgkmcnt(0)
	v_mbcnt_lo_u32_b32 v0, -1, 0
	v_mbcnt_hi_u32_b32 v0, -1, v0
	s_waitcnt vmcnt(0) lgkmcnt(0)
	s_barrier
	v_lshlrev_b32_e32 v5, 4, v0
	v_lshlrev_b32_e32 v4, 3, v0
	v_and_b32_e32 v6, 0xc0, v5
	v_lshlrev_b32_e32 v7, 1, v0
	v_and_or_b32 v6, v4, 24, v6
	v_and_b32_e32 v8, 32, v7
	v_and_b32_e32 v4, 0x100, v4
	v_or3_b32 v137, v6, v8, v4
	v_add_u32_e32 v4, s40, v5
	v_bfe_u32 v8, v0, 2, 2
	v_lshrrev_b32_e32 v9, 1, v0
	v_and_b32_e32 v6, 15, v0
	v_and_or_b32 v8, v9, 8, v8
	v_ashrrev_i32_e32 v9, 8, v4
	v_bitop3_b32 v10, v9, v6, 7 bitop3:0x6c
	v_lshlrev_b32_e32 v11, 10, v9
	v_lshl_or_b32 v132, v10, 4, v11
	v_and_b32_e32 v10, 0xfffff0, v9
	v_lshrrev_b32_e32 v9, 1, v9
	v_and_b32_e32 v9, 4, v9
	v_or3_b32 v9, v10, v9, v8
	v_and_b32_e32 v5, 48, v5
	v_and_b32_e32 v7, 0xc0, v7
	v_mul_i32_i24_e32 v9, 0x6a00, v9
	v_add_u32_e32 v4, 0x400, v4
	v_or3_b32 v133, v9, v7, v5
	v_ashrrev_i32_e32 v7, 8, v4
	v_bitop3_b32 v6, v7, v6, 7 bitop3:0x6c
	v_lshlrev_b32_e32 v9, 10, v7
	v_lshl_or_b32 v134, v6, 4, v9
	v_and_b32_e32 v6, 0xfffff0, v7
	v_lshrrev_b32_e32 v7, 1, v7
	v_and_b32_e32 v7, 4, v7
	v_or3_b32 v6, v6, v7, v8
	v_lshrrev_b32_e32 v4, 3, v4
	v_and_b32_e32 v138, 31, v0
	v_lshrrev_b32_e32 v1, 5, v0
	v_bfe_u32 v139, v0, 5, 1
	v_and_b32_e32 v4, 0xc0, v4
	v_mul_i32_i24_e32 v6, 0x6a00, v6
	v_or3_b32 v135, v6, v4, v5
	v_xor_b32_e32 v0, v1, v0
	v_lshlrev_b32_e32 v1, 4, v138
	v_lshlrev_b32_e32 v141, 2, v139
	v_cndmask_b32_e64 v4, 0, 1, s[10:11]
	v_add_u32_e32 v136, 0, v137
	v_lshlrev_b32_e32 v152, 8, v138
	v_lshlrev_b32_e32 v154, 4, v0
	v_and_b32_e32 v153, 0x60, v1
	v_bitop3_b32 v151, v1, 32, v166 bitop3:0x6c
	v_bitop3_b32 v150, v1, 64, v166 bitop3:0x6c
	v_bitop3_b32 v143, v1, s70, v1 bitop3:0xc
	v_sub_u32_e32 v142, v163, v141
	v_cmp_ne_u32_e64 s[10:11], 1, v4
	s_cbranch_vccz .LBB0_2005
	v_and_b32_e32 v0, 16, v154
	v_add3_u32 v0, 0, v152, v0
	s_waitcnt vmcnt(0) lgkmcnt(0)
	s_barrier
	v_add_u32_e32 v155, v0, v153
	ds_read_b128 v[4:7], v155 offset:32768
	v_add_u32_e32 v170, v0, v151
	v_add_u32_e32 v171, v0, v150
	v_add_u32_e32 v172, v0, v143
	v_cmp_lt_i32_e64 s[12:13], 0, v142
	v_cmp_lt_i32_e64 s[14:15], 32, v142
	s_waitcnt lgkmcnt(0)
	v_mfma_f32_32x32x16_bf16 v[20:35], v[4:7], v[100:103], 0
	ds_read_b128 v[4:7], v155 offset:40960
	v_cmp_lt_i32_e64 s[16:17], 1, v142
	v_cmp_lt_i32_e64 s[18:19], 33, v142
	v_cmp_lt_i32_e64 s[20:21], 2, v142
	v_cmp_lt_i32_e64 s[22:23], 34, v142
	v_cmp_lt_i32_e64 s[24:25], 3, v142
	v_cmp_lt_i32_e64 s[26:27], 35, v142
	s_waitcnt lgkmcnt(0)
	v_mfma_f32_32x32x16_bf16 v[36:51], v[4:7], v[100:103], 0
	ds_read_b128 v[4:7], v170 offset:32768
	v_cmp_lt_i32_e64 s[28:29], 8, v142
	v_cmp_lt_i32_e64 s[30:31], 40, v142
	v_cmp_lt_i32_e64 s[34:35], 9, v142
	v_cmp_lt_i32_e64 s[36:37], 41, v142
	v_cmp_lt_i32_e64 s[38:39], 10, v142
	v_cmp_lt_i32_e64 s[40:41], 42, v142
	s_waitcnt lgkmcnt(0)
	v_mfma_f32_32x32x16_bf16 v[20:35], v[4:7], v[108:111], v[20:35]
	ds_read_b128 v[4:7], v170 offset:40960
	v_cmp_lt_i32_e64 s[42:43], 11, v142
	v_cmp_lt_i32_e64 s[44:45], 43, v142
	v_cmp_lt_i32_e64 s[46:47], 16, v142
	v_cmp_lt_i32_e64 s[48:49], 48, v142
	v_cmp_lt_i32_e64 s[50:51], 17, v142
	v_cmp_lt_i32_e64 s[52:53], 49, v142
	s_waitcnt lgkmcnt(0)
	v_mfma_f32_32x32x16_bf16 v[36:51], v[4:7], v[108:111], v[36:51]
	ds_read_b128 v[4:7], v171 offset:32768
	v_cmp_lt_i32_e64 s[54:55], 18, v142
	v_cmp_lt_i32_e64 s[56:57], 50, v142
	v_cmp_lt_i32_e64 s[58:59], 19, v142
	v_cmp_lt_i32_e64 s[60:61], 51, v142
	v_cmp_lt_i32_e64 s[62:63], 24, v142
	v_cmp_lt_i32_e64 s[64:65], 56, v142
	s_waitcnt lgkmcnt(0)
	v_mfma_f32_32x32x16_bf16 v[20:35], v[4:7], v[116:119], v[20:35]
	ds_read_b128 v[4:7], v171 offset:40960
	v_cmp_lt_i32_e64 s[66:67], 25, v142
	v_cmp_lt_i32_e64 s[68:69], 57, v142
	v_cmp_lt_i32_e64 s[70:71], 26, v142
	v_cmp_lt_i32_e64 s[72:73], 58, v142
	v_cmp_lt_i32_e64 s[74:75], 27, v142
	v_cmp_lt_i32_e64 s[76:77], 59, v142
	s_waitcnt lgkmcnt(0)
	v_mfma_f32_32x32x16_bf16 v[36:51], v[4:7], v[116:119], v[36:51]
	ds_read_b128 v[4:7], v172 offset:32768
	s_and_b64 vcc, exec, s[10:11]
	s_waitcnt lgkmcnt(0)
	v_mfma_f32_32x32x16_bf16 v[20:35], v[4:7], v[124:127], v[20:35]
	ds_read_b128 v[4:7], v172 offset:40960
	s_waitcnt lgkmcnt(0)
	v_mfma_f32_32x32x16_bf16 v[36:51], v[4:7], v[124:127], v[36:51]
	ds_read_b128 v[4:7], v155 offset:32896
	s_waitcnt lgkmcnt(0)
	v_mfma_f32_32x32x16_bf16 v[20:35], v[4:7], v[104:107], v[20:35]
	ds_read_b128 v[4:7], v155 offset:41088
	s_waitcnt lgkmcnt(0)
	v_mfma_f32_32x32x16_bf16 v[36:51], v[4:7], v[104:107], v[36:51]
	ds_read_b128 v[4:7], v170 offset:32896
	ds_read_b128 v[8:11], v172 offset:41088
	ds_read_b128 v[12:15], v172 offset:32896
	ds_read_b128 v[16:19], v170 offset:41088
	s_waitcnt lgkmcnt(3)
	v_mfma_f32_32x32x16_bf16 v[20:35], v[4:7], v[112:115], v[20:35]
	ds_read_b128 v[4:7], v171 offset:41088
	ds_read_b128 v[52:55], v171 offset:32896
	s_waitcnt lgkmcnt(2)
	v_mfma_f32_32x32x16_bf16 v[36:51], v[16:19], v[112:115], v[36:51]
	s_waitcnt lgkmcnt(0)
	v_mfma_f32_32x32x16_bf16 v[20:35], v[52:55], v[120:123], v[20:35]
	v_mfma_f32_32x32x16_bf16 v[36:51], v[4:7], v[120:123], v[36:51]
	v_mfma_f32_32x32x16_bf16 v[20:35], v[12:15], v[128:131], v[20:35]
	v_mfma_f32_32x32x16_bf16 v[36:51], v[8:11], v[128:131], v[36:51]
	s_cbranch_vccnz .LBB0_1917
	s_nop 9
	v_cndmask_b32_e64 v20, v168, v20, s[12:13]
	v_cndmask_b32_e64 v36, v168, v36, s[14:15]
	v_cndmask_b32_e64 v21, v168, v21, s[16:17]
	v_cndmask_b32_e64 v37, v168, v37, s[18:19]
	v_cndmask_b32_e64 v22, v168, v22, s[20:21]
	v_cndmask_b32_e64 v38, v168, v38, s[22:23]
	v_cndmask_b32_e64 v23, v168, v23, s[24:25]
	v_cndmask_b32_e64 v39, v168, v39, s[26:27]
	v_cndmask_b32_e64 v24, v168, v24, s[28:29]
	v_cndmask_b32_e64 v40, v168, v40, s[30:31]
	v_cndmask_b32_e64 v25, v168, v25, s[34:35]
	v_cndmask_b32_e64 v41, v168, v41, s[36:37]
	v_cndmask_b32_e64 v26, v168, v26, s[38:39]
	v_cndmask_b32_e64 v42, v168, v42, s[40:41]
	v_cndmask_b32_e64 v27, v168, v27, s[42:43]
	v_cndmask_b32_e64 v43, v168, v43, s[44:45]
	v_cndmask_b32_e64 v28, v168, v28, s[46:47]
	v_cndmask_b32_e64 v44, v168, v44, s[48:49]
	v_cndmask_b32_e64 v29, v168, v29, s[50:51]
	v_cndmask_b32_e64 v45, v168, v45, s[52:53]
	v_cndmask_b32_e64 v30, v168, v30, s[54:55]
	v_cndmask_b32_e64 v46, v168, v46, s[56:57]
	v_cndmask_b32_e64 v31, v168, v31, s[58:59]
	v_cndmask_b32_e64 v47, v168, v47, s[60:61]
	v_cndmask_b32_e64 v32, v168, v32, s[62:63]
	v_cndmask_b32_e64 v48, v168, v48, s[64:65]
	v_cndmask_b32_e64 v33, v168, v33, s[66:67]
	v_cndmask_b32_e64 v49, v168, v49, s[68:69]
	v_cndmask_b32_e64 v34, v168, v34, s[70:71]
	v_cndmask_b32_e64 v50, v168, v50, s[72:73]
	v_cndmask_b32_e64 v35, v168, v35, s[74:75]
	v_cndmask_b32_e64 v51, v168, v51, s[76:77]
